# top-k bisection: 6 of the 8 per-lane carry adds per counting block as scalar popcounts (was 4) - stacked on v23
# speedup vs baseline: 1.0011x; 1.0011x over previous
.LBB0_417:
	v_lshlrev_b32_e64 v131, v123, 1
	v_or_b32_e32 v131, v71, v131
	v_mov_b32_e32 v133, 0
	s_mov_b32 s98, 0
	s_andn2_b64 vcc, exec, s[44:45]
	v_cmp_ge_u32_e64 s[80:81], v111, v131
	v_cmp_ge_u32_e64 s[82:83], v130, v131
	v_cmp_ge_u32_e64 s[84:85], v109, v131
	v_cmp_ge_u32_e64 s[86:87], v1, v131
	v_cmp_ge_u32_e64 s[88:89], v2, v131
	v_cmp_ge_u32_e64 s[90:91], v129, v131
	v_cmp_ge_u32_e64 s[92:93], v128, v131
	v_cmp_ge_u32_e64 s[94:95], v127, v131
	v_addc_co_u32_e64 v133, s[96:97], 0, v133, s[80:81]
	v_addc_co_u32_e64 v133, s[96:97], 0, v133, s[82:83]
	s_bcnt1_i32_b64 s99, s[84:85]
	s_add_i32 s98, s98, s99
	s_bcnt1_i32_b64 s99, s[86:87]
	s_add_i32 s98, s98, s99
	s_bcnt1_i32_b64 s99, s[88:89]
	s_add_i32 s98, s98, s99
	s_bcnt1_i32_b64 s99, s[90:91]
	s_add_i32 s98, s98, s99
	s_bcnt1_i32_b64 s99, s[92:93]
	s_add_i32 s98, s98, s99
	s_bcnt1_i32_b64 s99, s[94:95]
	s_add_i32 s98, s98, s99
	s_cbranch_vccnz .LBB0_421
	v_cmp_ge_u32_e64 s[80:81], v4, v131
	v_cmp_ge_u32_e64 s[82:83], v126, v131
	v_cmp_ge_u32_e64 s[84:85], v125, v131
	v_cmp_ge_u32_e64 s[86:87], v124, v131
	v_cmp_ge_u32_e64 s[88:89], v122, v131
	v_cmp_ge_u32_e64 s[90:91], v121, v131
	v_cmp_ge_u32_e64 s[92:93], v120, v131
	v_cmp_ge_u32_e64 s[94:95], v119, v131
	v_addc_co_u32_e64 v133, s[96:97], 0, v133, s[80:81]
	v_addc_co_u32_e64 v133, s[96:97], 0, v133, s[82:83]
	s_bcnt1_i32_b64 s99, s[84:85]
	s_add_i32 s98, s98, s99
	s_bcnt1_i32_b64 s99, s[86:87]
	s_add_i32 s98, s98, s99
	s_bcnt1_i32_b64 s99, s[88:89]
	s_add_i32 s98, s98, s99
	s_bcnt1_i32_b64 s99, s[90:91]
	s_add_i32 s98, s98, s99
	s_bcnt1_i32_b64 s99, s[92:93]
	s_add_i32 s98, s98, s99
	s_bcnt1_i32_b64 s99, s[94:95]
	s_add_i32 s98, s98, s99
	s_andn2_b64 vcc, exec, s[60:61]
	s_cbranch_vccz .LBB0_422

.LBB0_420:
	v_cmp_ge_u32_e64 s[80:81], v102, v131
	v_cmp_ge_u32_e64 s[82:83], v100, v131
	v_cmp_ge_u32_e64 s[84:85], v99, v131
	v_cmp_ge_u32_e64 s[86:87], v98, v131
	v_cmp_ge_u32_e64 s[88:89], v97, v131
	v_cmp_ge_u32_e64 s[90:91], v96, v131
	v_cmp_ge_u32_e64 s[92:93], v95, v131
	v_cmp_ge_u32_e64 s[94:95], v94, v131
	v_addc_co_u32_e64 v133, s[96:97], 0, v133, s[80:81]
	v_addc_co_u32_e64 v133, s[96:97], 0, v133, s[82:83]
	s_bcnt1_i32_b64 s99, s[84:85]
	s_add_i32 s98, s98, s99
	s_bcnt1_i32_b64 s99, s[86:87]
	s_add_i32 s98, s98, s99
	s_bcnt1_i32_b64 s99, s[88:89]
	s_add_i32 s98, s98, s99
	s_bcnt1_i32_b64 s99, s[90:91]
	s_add_i32 s98, s98, s99
	s_bcnt1_i32_b64 s99, s[92:93]
	s_add_i32 s98, s98, s99
	s_bcnt1_i32_b64 s99, s[94:95]
	s_add_i32 s98, s98, s99
	s_nop 0
	v_cmp_ge_u32_e64 s[80:81], v93, v131
	v_cmp_ge_u32_e64 s[82:83], v92, v131
	v_cmp_ge_u32_e64 s[84:85], v91, v131
	v_cmp_ge_u32_e64 s[86:87], v90, v131
	v_cmp_ge_u32_e64 s[88:89], v89, v131
	v_cmp_ge_u32_e64 s[90:91], v88, v131
	v_cmp_ge_u32_e64 s[92:93], v87, v131
	v_cmp_ge_u32_e64 s[94:95], v86, v131
	v_addc_co_u32_e64 v133, s[96:97], 0, v133, s[80:81]
	v_addc_co_u32_e64 v133, s[96:97], 0, v133, s[82:83]
	s_bcnt1_i32_b64 s99, s[84:85]
	s_add_i32 s98, s98, s99
	s_bcnt1_i32_b64 s99, s[86:87]
	s_add_i32 s98, s98, s99
	s_bcnt1_i32_b64 s99, s[88:89]
	s_add_i32 s98, s98, s99
	s_bcnt1_i32_b64 s99, s[90:91]
	s_add_i32 s98, s98, s99
	s_bcnt1_i32_b64 s99, s[92:93]
	s_add_i32 s98, s98, s99
	s_bcnt1_i32_b64 s99, s[94:95]
	s_add_i32 s98, s98, s99
	s_andn2_b64 vcc, exec, s[48:49]
	s_cbranch_vccnz .LBB0_416
	s_branch .LBB0_424

.LBB0_422:
	v_cmp_ge_u32_e64 s[80:81], v5, v131
	v_cmp_ge_u32_e64 s[82:83], v118, v131
	v_cmp_ge_u32_e64 s[84:85], v117, v131
	v_cmp_ge_u32_e64 s[86:87], v116, v131
	v_cmp_ge_u32_e64 s[88:89], v115, v131
	v_cmp_ge_u32_e64 s[90:91], v114, v131
	v_cmp_ge_u32_e64 s[92:93], v113, v131
	v_cmp_ge_u32_e64 s[94:95], v112, v131
	v_addc_co_u32_e64 v133, s[96:97], 0, v133, s[80:81]
	v_addc_co_u32_e64 v133, s[96:97], 0, v133, s[82:83]
	s_bcnt1_i32_b64 s99, s[84:85]
	s_add_i32 s98, s98, s99
	s_bcnt1_i32_b64 s99, s[86:87]
	s_add_i32 s98, s98, s99
	s_bcnt1_i32_b64 s99, s[88:89]
	s_add_i32 s98, s98, s99
	s_bcnt1_i32_b64 s99, s[90:91]
	s_add_i32 s98, s98, s99
	s_bcnt1_i32_b64 s99, s[92:93]
	s_add_i32 s98, s98, s99
	s_bcnt1_i32_b64 s99, s[94:95]
	s_add_i32 s98, s98, s99
	s_nop 0
	v_cmp_ge_u32_e64 s[80:81], v110, v131
	v_cmp_ge_u32_e64 s[82:83], v108, v131
	v_cmp_ge_u32_e64 s[84:85], v107, v131
	v_cmp_ge_u32_e64 s[86:87], v106, v131
	v_cmp_ge_u32_e64 s[88:89], v105, v131
	v_cmp_ge_u32_e64 s[90:91], v104, v131
	v_cmp_ge_u32_e64 s[92:93], v103, v131
	v_cmp_ge_u32_e64 s[94:95], v101, v131
	v_addc_co_u32_e64 v133, s[96:97], 0, v133, s[80:81]
	v_addc_co_u32_e64 v133, s[96:97], 0, v133, s[82:83]
	s_bcnt1_i32_b64 s99, s[84:85]
	s_add_i32 s98, s98, s99
	s_bcnt1_i32_b64 s99, s[86:87]
	s_add_i32 s98, s98, s99
	s_bcnt1_i32_b64 s99, s[88:89]
	s_add_i32 s98, s98, s99
	s_bcnt1_i32_b64 s99, s[90:91]
	s_add_i32 s98, s98, s99
	s_bcnt1_i32_b64 s99, s[92:93]
	s_add_i32 s98, s98, s99
	s_bcnt1_i32_b64 s99, s[94:95]
	s_add_i32 s98, s98, s99
	s_andn2_b64 vcc, exec, s[12:13]
	s_cbranch_vccz .LBB0_420

.LBB0_424:
	v_cmp_ge_u32_e64 s[80:81], v132, v131
	v_cmp_ge_u32_e64 s[82:83], v85, v131
	v_cmp_ge_u32_e64 s[84:85], v84, v131
	v_cmp_ge_u32_e64 s[86:87], v83, v131
	v_cmp_ge_u32_e64 s[88:89], v82, v131
	v_cmp_ge_u32_e64 s[90:91], v81, v131
	v_cmp_ge_u32_e64 s[92:93], v80, v131
	v_cmp_ge_u32_e64 s[94:95], v79, v131
	v_addc_co_u32_e64 v133, s[96:97], 0, v133, s[80:81]
	v_addc_co_u32_e64 v133, s[96:97], 0, v133, s[82:83]
	s_bcnt1_i32_b64 s99, s[84:85]
	s_add_i32 s98, s98, s99
	s_bcnt1_i32_b64 s99, s[86:87]
	s_add_i32 s98, s98, s99
	s_bcnt1_i32_b64 s99, s[88:89]
	s_add_i32 s98, s98, s99
	s_bcnt1_i32_b64 s99, s[90:91]
	s_add_i32 s98, s98, s99
	s_bcnt1_i32_b64 s99, s[92:93]
	s_add_i32 s98, s98, s99
	s_bcnt1_i32_b64 s99, s[94:95]
	s_add_i32 s98, s98, s99
	s_nop 0
	v_cmp_ge_u32_e64 s[80:81], v78, v131
	v_cmp_ge_u32_e64 s[82:83], v77, v131
	v_cmp_ge_u32_e64 s[84:85], v76, v131
	v_cmp_ge_u32_e64 s[86:87], v75, v131
	v_cmp_ge_u32_e64 s[88:89], v74, v131
	v_cmp_ge_u32_e64 s[90:91], v73, v131
	v_cmp_ge_u32_e64 s[92:93], v72, v131
	v_cmp_ge_u32_e64 s[94:95], v70, v131
	v_addc_co_u32_e64 v133, s[96:97], 0, v133, s[80:81]
	v_addc_co_u32_e64 v133, s[96:97], 0, v133, s[82:83]
	s_bcnt1_i32_b64 s99, s[84:85]
	s_add_i32 s98, s98, s99
	s_bcnt1_i32_b64 s99, s[86:87]
	s_add_i32 s98, s98, s99
	s_bcnt1_i32_b64 s99, s[88:89]
	s_add_i32 s98, s98, s99
	s_bcnt1_i32_b64 s99, s[90:91]
	s_add_i32 s98, s98, s99
	s_bcnt1_i32_b64 s99, s[92:93]
	s_add_i32 s98, s98, s99
	s_bcnt1_i32_b64 s99, s[94:95]
	s_add_i32 s98, s98, s99
	s_branch .LBB0_416
